# speedup vs baseline: 1.0075x; 1.0075x over previous
_Z6k_dlrmPKiS0_S0_S0_S0_S0_S0_PKfS2_S2_S2_S2_S2_S2_S2_S2_S2_S2_S2_S2_S2_S2_S2_Pf:
	v_readfirstlane_b32 s33, v0
	s_load_dwordx16 s[40:55], s[0:1], 0x0
	s_load_dwordx16 s[56:71], s[0:1], 0x40
	s_load_dwordx16 s[72:87], s[0:1], 0x80
	s_lshr_b32 s37, s33, 6
	s_lshl_b32 s30, s2, 6
	s_lshl_b32 s34, s37, 2
	v_and_b32_e32 v1, 63, v0
	s_add_i32 s6, s34, s30
	v_lshl_or_b32 v2, s6, 6, v1
	v_ashrrev_i32_e32 v3, 31, v2
	v_and_b32_e32 v17, 31, v0
	v_and_b32_e32 v82, 15, v0
	s_waitcnt lgkmcnt(0)
	s_load_dword s88, s[84:85], 0x0
	v_lshl_add_u64 v[2:3], v[2:3], 2, s[50:51]
	global_load_dword v10, v[2:3], off
	global_load_dword v11, v[2:3], off offset:256
	global_load_dword v12, v[2:3], off offset:512
	global_load_dword v14, v[2:3], off offset:768
	v_lshl_or_b32 v2, s6, 3, v17
	v_ashrrev_i32_e32 v3, 31, v2
	v_lshl_add_u64 v[2:3], v[2:3], 2, s[46:47]
	global_load_dword v13, v[2:3], off
	v_cmp_gt_u32_e32 vcc, 4, v1
	v_mov_b32_e32 v15, 0
	v_mov_b32_e32 v5, 0
	v_mov_b32_e32 v4, 0
	v_mov_b32_e32 v3, 0
	v_mov_b32_e32 v2, 0
	s_and_saveexec_b64 s[2:3], vcc
	v_or_b32_e32 v2, s6, v1
	v_ashrrev_i32_e32 v3, 31, v2
	v_lshlrev_b64 v[6:7], 2, v[2:3]
	v_lshl_add_u64 v[2:3], s[52:53], 0, v[6:7]
	v_lshl_add_u64 v[4:5], s[48:49], 0, v[6:7]
	global_load_dword v2, v[2:3], off
	v_lshl_add_u64 v[8:9], s[42:43], 0, v[6:7]
	global_load_dword v3, v[4:5], off
	v_lshl_add_u64 v[4:5], s[40:41], 0, v[6:7]
	v_lshl_add_u64 v[6:7], s[44:45], 0, v[6:7]
	global_load_dword v4, v[4:5], off
	s_nop 0
	global_load_dword v5, v[8:9], off
	global_load_dword v15, v[6:7], off
	s_or_b64 exec, exec, s[2:3]
	v_or_b32_e32 v6, s30, v1
	v_ashrrev_i32_e32 v7, 31, v6
	v_lshl_add_u64 v[6:7], v[6:7], 2, s[54:55]
	global_load_dword v16, v[6:7], off
	s_cmp_lt_u32 s37, 4
	s_cbranch_scc1 .Lpro_wl_done
	v_lshrrev_b32_e32 v20, 5, v1
	v_lshlrev_b32_e32 v21, 2, v17
	v_lshl_or_b32 v22, v20, 12, v21
	v_lshl_or_b32 v23, v20, 10, v21
	v_lshrrev_b32_e32 v24, 4, v1
	v_lshlrev_b32_e32 v25, 2, v82
	v_lshl_or_b32 v24, v24, 11, v25
	v_lshlrev_b32_e32 v26, 2, v1
	s_sub_i32 s89, s37, 4
	s_mul_i32 s90, s89, 13
	s_lshr_b32 s90, s90, 6
	s_mul_i32 s91, s90, 5
	s_sub_i32 s91, s89, s91
	s_lshl_b32 s38, s91, 4
	s_add_i32 s38, s38, 15
	s_cmp_lt_u32 s91, 4
	s_cselect_b32 s38, s38, 0
	s_mov_b32 s92, 0
	s_cselect_b32 s93, 0, -1
	s_lshl_b32 s38, s38, 9
	s_lshl_b32 s90, s90, 7
	s_add_u32 s38, s38, s90
	s_add_u32 s90, s74, s38
	s_addc_u32 s91, s75, 0
	global_load_dword v84, v22, s[90:91]
	global_load_dword v85, v22, s[90:91] offset:512
	global_load_dword v86, v22, s[90:91] offset:1024
	global_load_dword v87, v22, s[90:91] offset:1536
	global_load_dword v88, v22, s[90:91] offset:2048
	global_load_dword v89, v22, s[90:91] offset:2560
	global_load_dword v90, v22, s[90:91] offset:3072
	global_load_dword v91, v22, s[90:91] offset:3584
	s_cmp_lt_u32 s37, 12
	s_cbranch_scc0 .Lpro_r1_w2
	s_add_i32 s89, s37, 8
	s_mul_i32 s90, s89, 13
	s_lshr_b32 s90, s90, 6
	s_mul_i32 s91, s90, 5
	s_sub_i32 s91, s89, s91
	s_lshl_b32 s38, s91, 4
	s_add_i32 s38, s38, 15
	s_cmp_lt_u32 s91, 4
	s_cselect_b32 s38, s38, 0
	s_mov_b32 s94, 0
	s_cselect_b32 s95, 0, -1
	s_lshl_b32 s38, s38, 9
	s_lshl_b32 s90, s90, 7
	s_add_u32 s38, s38, s90
	s_add_u32 s90, s74, s38
	s_addc_u32 s91, s75, 0
	global_load_dword v92, v22, s[90:91]
	global_load_dword v93, v22, s[90:91] offset:512
	global_load_dword v94, v22, s[90:91] offset:1024
	global_load_dword v95, v22, s[90:91] offset:1536
	global_load_dword v96, v22, s[90:91] offset:2048
	global_load_dword v97, v22, s[90:91] offset:2560
	global_load_dword v98, v22, s[90:91] offset:3072
	global_load_dword v99, v22, s[90:91] offset:3584
	s_branch .Lpro_r1_done
.Lpro_r1_w2:
	s_sub_i32 s89, s37, 12
	s_lshl_b32 s38, s89, 12
	s_mov_b32 s94, 0
	s_mov_b32 s95, 0
	s_add_u32 s90, s78, s38
	s_addc_u32 s91, s79, 0
	global_load_dword v92, v23, s[90:91]
	global_load_dword v93, v23, s[90:91] offset:256
	global_load_dword v94, v23, s[90:91] offset:512
	global_load_dword v95, v23, s[90:91] offset:768
	global_load_dword v96, v23, s[90:91] offset:2048
	global_load_dword v97, v23, s[90:91] offset:2304
	global_load_dword v98, v23, s[90:91] offset:2560
	global_load_dword v99, v23, s[90:91] offset:2816
.Lpro_r1_done:
	s_lshr_b32 s90, s37, 3
	s_and_b32 s38, s37, 7
	s_lshl_b32 s38, s38, 12
	s_lshl_b32 s90, s90, 7
	s_add_u32 s38, s38, s90
	s_add_u32 s90, s78, s38
	s_addc_u32 s91, s79, 0
	global_load_dword v100, v23, s[90:91]
	global_load_dword v101, v23, s[90:91] offset:256
	global_load_dword v102, v23, s[90:91] offset:512
	global_load_dword v103, v23, s[90:91] offset:768
	global_load_dword v104, v23, s[90:91] offset:2048
	global_load_dword v105, v23, s[90:91] offset:2304
	global_load_dword v108, v23, s[90:91] offset:2560
	global_load_dword v109, v23, s[90:91] offset:2816
	s_cmp_lt_u32 s37, 12
	s_cbranch_scc0 .Lpro_r3_done
	s_sub_i32 s89, s37, 4
	s_lshr_b32 s90, s89, 1
	s_and_b32 s38, s89, 1
	s_lshl_b32 s38, s38, 13
	s_lshl_b32 s90, s90, 6
	s_add_u32 s38, s38, s90
	s_add_u32 s90, s70, s38
	s_addc_u32 s91, s71, 0
	global_load_dword v110, v24, s[90:91]
	global_load_dword v111, v24, s[90:91] offset:256
	global_load_dword v112, v24, s[90:91] offset:512
	global_load_dword v113, v24, s[90:91] offset:768
	global_load_dword v114, v24, s[90:91] offset:1024
	global_load_dword v115, v24, s[90:91] offset:1280
	global_load_dword v116, v24, s[90:91] offset:1536
	global_load_dword v117, v24, s[90:91] offset:1792
.Lpro_r3_done:
	s_cmp_lt_u32 s37, 11
	s_cbranch_scc0 .Lpro_wl_done
	s_sub_i32 s89, s37, 4
	s_mov_b64 s[90:91], s[76:77]
	s_cmp_eq_u32 s89, 2
	s_cselect_b64 s[90:91], s[80:81], s[90:91]
	s_cmp_eq_u32 s89, 3
	s_cselect_b64 s[90:91], s[82:83], s[90:91]
	s_cmp_eq_u32 s89, 4
	s_cselect_b64 s[90:91], s[66:67], s[90:91]
	s_cmp_eq_u32 s89, 5
	s_cselect_b64 s[90:91], s[68:69], s[90:91]
	s_cmp_eq_u32 s89, 6
	s_cselect_b64 s[90:91], s[72:73], s[90:91]
	s_cmp_eq_u32 s89, 1
	s_cselect_b32 s38, 0x100, 0
	s_add_u32 s90, s90, s38
	s_addc_u32 s91, s91, 0
	global_load_dword v118, v26, s[90:91]
.Lpro_wl_done:
	s_waitcnt vmcnt(0)
	s_cmp_lg_u32 s37, 0
	s_cbranch_scc1 .Lpro_not_w0
	v_mov_b32_e32 v6, 0x15300
	v_lshl_add_u32 v6, v1, 2, v6
	ds_write_b32 v6, v16
	v_mov_b32_e32 v6, 0
	v_mov_b32_e32 v7, 0x15400
	ds_write_b32 v7, v6
.Lpro_not_w0:
	v_cmp_gt_u32_e32 vcc, 4, v1
	s_lshl_b32 s6, s37, 10
	v_lshlrev_b32_e32 v6, 6, v0
	s_lshl_b32 s7, s37, 7
	s_add_i32 s6, s6, 0xf400
	v_and_b32_e32 v6, 0xc0, v6
	v_and_b32_e32 v7, 60, v1
	s_lshl_b32 s31, s37, 5
	s_add_i32 s7, s7, 0x13c00
	v_or3_b32 v6, s6, v6, v7
	v_cmp_gt_u32_e64 s[2:3], 32, v1
	ds_write2st64_b32 v6, v10, v11 offset1:1
	ds_write2st64_b32 v6, v12, v14 offset0:2 offset1:3
	s_and_saveexec_b64 s[4:5], s[2:3]
	v_lshl_add_u32 v6, v1, 2, s7
	ds_write_b32 v6, v13
	s_or_b64 exec, exec, s[4:5]
	s_mov_b64 s[14:15], s[60:61]
	s_mov_b64 s[24:25], s[56:57]
	s_mov_b64 s[26:27], s[58:59]
	s_lshl_b32 s8, s31, 2
	s_add_i32 s8, s8, 0x14400
	s_and_saveexec_b64 s[2:3], vcc
	s_cbranch_execz .LBB0_32
	v_lshl_add_u32 v6, v1, 5, s8
	ds_write_b128 v6, v[2:5]
	ds_write_b32 v6, v15 offset:16

.LBB0_34:
	s_or_b64 exec, exec, s[4:5]
	s_mov_b64 s[18:19], s[62:63]
	v_cmp_le_i32_e32 vcc, s36, v106
	s_and_saveexec_b64 s[2:3], vcc
	s_xor_b64 s[2:3], exec, s[2:3]
	v_lshlrev_b32_e32 v107, 4, v82
	s_or_saveexec_b64 s[2:3], s[2:3]
	v_mov_b32_e32 v10, 0
	v_mov_b32_e32 v11, v10
	v_mov_b32_e32 v12, v10
	v_mov_b32_e32 v13, v10
	v_mov_b64_e32 v[6:7], v[10:11]
	v_mov_b64_e32 v[8:9], v[12:13]
	s_xor_b64 exec, exec, s[2:3]
	s_cbranch_execz .LBB0_38
	v_lshl_or_b32 v6, v14, 8, v107
	s_waitcnt lgkmcnt(0)
	global_load_dwordx4 v[6:9], v6, s[18:19]
.LBB0_38:
	s_or_b64 exec, exec, s[2:3]
	s_mov_b64 s[28:29], s[64:65]
	s_add_i32 s2, s36, -4
	v_cmp_gt_i32_e32 vcc, s2, v106
	s_and_saveexec_b64 s[2:3], vcc
	s_cbranch_execz .LBB0_40
	v_lshl_or_b32 v10, v15, 8, v107
	s_waitcnt lgkmcnt(0)
	global_load_dwordx4 v[10:13], v10, s[18:19]

.LBB0_44:
	s_or_b64 exec, exec, s[2:3]
	v_mov_b32_e32 v26, 0
	v_mov_b32_e32 v27, v26
	s_add_i32 s2, s35, -8
	s_waitcnt lgkmcnt(0)
	v_mov_b32_e32 v28, v26
	v_mov_b32_e32 v29, v26
	v_mov_b64_e32 v[22:23], v[26:27]
	v_cmp_gt_i32_e32 vcc, s2, v106
	v_mov_b64_e32 v[24:25], v[28:29]
	s_and_saveexec_b64 s[2:3], vcc
	s_cbranch_execz .LBB0_46
	v_lshl_or_b32 v22, v30, 8, v107
	global_load_dwordx4 v[22:25], v22, s[28:29] nt

.LBB0_70:
	s_or_b64 exec, exec, s[2:3]
	s_mov_b64 s[20:21], s[84:85]
	s_mov_b64 s[22:23], s[86:87]
	s_sub_i32 s0, s35, 60
	v_cmp_gt_i32_e32 vcc, s0, v106
	s_and_saveexec_b64 s[0:1], vcc
	s_cbranch_execz .LBB0_72
	s_waitcnt lgkmcnt(0)
	v_lshl_or_b32 v62, v65, 8, v107
	global_load_dwordx4 v[78:81], v62, s[28:29] nt
.LBB0_72:
	s_or_b64 exec, exec, s[0:1]
	s_cmp_lt_u32 s37, 4
	s_cbranch_scc1 .Lpro_wc_done
	v_lshlrev_b32_e32 v119, 4, v1
	s_sub_i32 s89, s37, 4
	s_lshl_b32 s38, s89, 10
	v_add_u32_e32 v119, s38, v119
	v_cndmask_b32_e64 v91, v91, 0, s[92:93]
	v_cvt_pk_f16_f32 v84, v84, v85
	v_cvt_pk_f16_f32 v85, v86, v87
	v_cvt_pk_f16_f32 v86, v88, v89
	v_cvt_pk_f16_f32 v87, v90, v91
	ds_write_b128 v119, v[84:87]
	v_cndmask_b32_e64 v99, v99, 0, s[94:95]
	v_cvt_pk_f16_f32 v92, v92, v93
	v_cvt_pk_f16_f32 v93, v94, v95
	v_cvt_pk_f16_f32 v94, v96, v97
	v_cvt_pk_f16_f32 v95, v98, v99
	ds_write_b128 v119, v[92:95] offset:12288
	v_cvt_pk_f16_f32 v100, v100, v101
	v_cvt_pk_f16_f32 v101, v102, v103
	v_cvt_pk_f16_f32 v102, v104, v105
	v_cvt_pk_f16_f32 v103, v108, v109
	ds_write_b128 v119, v[100:103] offset:24576
	s_cmp_lt_u32 s37, 12
	s_cbranch_scc0 .Lpro_wc_done
	v_cvt_pk_f16_f32 v110, v110, v111
	v_cvt_pk_f16_f32 v111, v112, v113
	v_cvt_pk_f16_f32 v112, v114, v115
	v_cvt_pk_f16_f32 v113, v116, v117
	ds_write_b128 v119, v[110:113] offset:36864
	s_cmp_lt_u32 s37, 11
	s_cbranch_scc0 .Lpro_wc_done
	s_lshl_b32 s38, s89, 8
	s_add_i32 s38, s38, 0x14c00
	v_lshl_add_u32 v119, v1, 2, s38
	ds_write_b32 v119, v118
.Lpro_wc_done:
	s_lshr_b32 s0, s33, 8
	s_lshl_b32 s1, s37, 4
	v_and_or_b32 v104, s1, 48, v82
	s_waitcnt lgkmcnt(0)
	v_mov_b32_e32 v62, 0x15300
	v_lshl_or_b32 v62, v104, 2, v62
	v_lshlrev_b32_e32 v109, 5, v106
	s_barrier
	ds_read_b32 v105, v62
	v_or_b32_e32 v62, 0x15000, v109
	v_or_b32_e32 v84, 0x15100, v109
	ds_read_b128 v[62:65], v62
	ds_read_b128 v[84:87], v84
	s_lshl_b32 s1, s0, 6
	s_add_i32 s2, s1, 0x14c00
	v_lshlrev_b32_e32 v108, 4, v106
	v_or_b32_e32 v88, s2, v108
	s_waitcnt lgkmcnt(0)
	v_fma_f32 v63, v105, v63, v85
	v_lshlrev_b32_e32 v92, 4, v1
	v_max_f32_e32 v101, 0, v63
	v_or_b32_e32 v63, 0x15010, v109
	ds_read_b128 v[88:91], v88 offset:1536
	v_lshl_or_b32 v100, s0, 11, v92
	v_fma_f32 v62, v105, v62, v84
	v_or_b32_e32 v84, 0x15110, v109
	ds_read_b128 v[92:95], v63
	ds_read_b128 v[96:99], v84
	v_fmac_f32_e32 v87, v105, v65
	v_fma_f32 v63, v105, v64, v86
	v_max_f32_e32 v102, 0, v87
	v_max_f32_e32 v62, 0, v62
	s_waitcnt lgkmcnt(0)
	v_fma_f32 v65, v105, v93, v97
	v_fma_f32 v64, v105, v92, v96
	v_max_f32_e32 v92, 0, v65
	v_fma_f32 v65, v105, v94, v98
	v_fmac_f32_e32 v99, v105, v95
	v_max_f32_e32 v65, 0, v65
	v_max_f32_e32 v84, 0, v99
	v_cvt_pk_f16_f32 v65, v65, v84
	ds_read_b128 v[84:87], v100 offset:36864
	v_max_f32_e32 v64, 0, v64
	v_cvt_pk_f16_f32 v64, v64, v92
	v_or_b32_e32 v92, 0x15080, v109
	v_or_b32_e32 v96, 0x15180, v109
	ds_read_b128 v[92:95], v92
	ds_read_b128 v[96:99], v96
	v_max_f32_e32 v63, 0, v63
	v_cvt_pk_f16_f32 v63, v63, v102
	v_cvt_pk_f16_f32 v62, v62, v101
	ds_read_b128 v[100:103], v100 offset:37888
	s_waitcnt lgkmcnt(1)
	v_fma_f32 v94, v105, v94, v98
	v_mfma_f32_16x16x32_f16 v[62:65], v[84:87], v[62:65], v[88:91]
	v_fma_f32 v84, v105, v92, v96
	v_max_f32_e32 v92, 0, v84
	v_fma_f32 v84, v105, v93, v97
	v_max_f32_e32 v93, 0, v84
	v_or_b32_e32 v84, 0x15090, v109
	v_or_b32_e32 v88, 0x15190, v109
	ds_read_b128 v[84:87], v84
	ds_read_b128 v[88:91], v88
	v_fmac_f32_e32 v99, v105, v95
	v_max_f32_e32 v94, 0, v94
	v_max_f32_e32 v95, 0, v99
	s_add_i32 s1, s1, 0xb000
	s_waitcnt lgkmcnt(0)
	v_fma_f32 v84, v105, v84, v88
	v_fma_f32 v85, v105, v85, v89
	v_fma_f32 v86, v105, v86, v90
	v_fmac_f32_e32 v91, v105, v87
	v_max_f32_e32 v84, 0, v84
	v_max_f32_e32 v85, 0, v85
	v_max_f32_e32 v86, 0, v86
	v_max_f32_e32 v87, 0, v91
	v_cvt_pk_f16_f32 v87, v86, v87
	v_cvt_pk_f16_f32 v86, v84, v85
	v_cvt_pk_f16_f32 v85, v94, v95
	v_cvt_pk_f16_f32 v84, v92, v93
	v_cmp_eq_u32_e64 s[12:13], 1, v106
	v_cmp_eq_u32_e64 s[2:3], 0, v1
	v_mfma_f32_16x16x32_f16 v[62:65], v[100:103], v[84:87], v[62:65]
	v_mul_u32_u24_e32 v84, 0x110, v104
	v_add3_u32 v84, s1, v84, v108
	v_or_b32_e32 v112, 4, v106
	v_or_b32_e32 v116, 60, v106
	s_nop 3
	ds_write_b128 v84, v[62:65]
	v_mbcnt_lo_u32_b32 v62, -1, 0
	v_mbcnt_hi_u32_b32 v62, -1, v62
	v_and_or_b32 v62, v62, 64, v82
	v_lshlrev_b32_e32 v108, 2, v62
	v_mov_b32_e32 v62, 0x13c00
	v_lshl_or_b32 v111, v106, 2, v62
	v_mov_b32_e32 v62, 0xf400
	v_lshl_or_b32 v113, v83, 2, v62
	v_and_b32_e32 v62, 8, v0
	v_cmp_eq_u32_e64 s[4:5], 0, v62
	v_and_b32_e32 v62, 4, v0
	v_cmp_eq_u32_e64 s[6:7], 0, v62
	v_and_b32_e32 v62, 2, v0
	v_and_b32_e32 v0, 1, v0
	v_cmp_eq_u32_e64 s[10:11], 0, v0
	v_mov_b32_e32 v0, 0x13400
	v_cmp_eq_u32_e64 s[8:9], 0, v62
	v_lshl_or_b32 v117, v1, 1, v0
	v_mov_b32_e32 v0, s14
	v_mov_b32_e32 v62, s26
	v_cndmask_b32_e64 v0, v0, v62, s[12:13]
	v_mov_b32_e32 v62, s15
	v_mov_b32_e32 v63, s27
	v_cndmask_b32_e64 v62, v62, v63, s[12:13]
	v_mov_b32_e32 v63, s25
	v_cmp_gt_u32_e64 s[14:15], 16, v1
	v_or_b32_e32 v109, 64, v108
	v_or_b32_e32 v110, 0x80, v108
	v_cndmask_b32_e64 v1, v62, v63, s[14:15]
	v_mov_b32_e32 v62, s24
	v_cndmask_b32_e64 v0, v0, v62, s[14:15]
	v_mov_b32_e32 v62, 0
	s_waitcnt lgkmcnt(0)
	s_barrier
	s_branch .LBB0_74

.LBB0_120:
	s_cmpk_gt_u32 s33, 0x7f
	s_waitcnt lgkmcnt(0)
	s_barrier
	s_cbranch_scc1 .LBB0_123
	v_mbcnt_lo_u32_b32 v92, -1, 0
	v_mbcnt_hi_u32_b32 v92, -1, v92
	v_mov_b32_e32 v1, 0x15300
	v_ashrrev_i32_e32 v0, 5, v92
	s_waitcnt vmcnt(0)
	v_and_or_b32 v37, v92, 31, s31
	v_lshlrev_b32_e32 v38, 4, v0
	v_lshl_add_u32 v1, v37, 2, v1
	v_add_u32_e32 v93, 0x14c00, v38
	ds_read_b32 v36, v1
	ds_read_b128 v[0:3], v93
	ds_read_b128 v[4:7], v93 offset:32
	ds_read_b128 v[8:11], v93 offset:64
	v_add_u32_e32 v39, v93, v38
	ds_read_b128 v[24:27], v39 offset:1280
	ds_read_b128 v[28:31], v39 offset:1024
	ds_read_b128 v[12:15], v93 offset:96
	ds_read_b128 v[16:19], v93 offset:128
	ds_read_b128 v[20:23], v39 offset:1040
	ds_read_b128 v[32:35], v39 offset:1232
	ds_read_b128 v[80:83], v93 offset:992
	s_waitcnt lgkmcnt(5)
	v_fma_f32 v24, v36, v28, v24
	v_max_f32_e32 v44, 0, v24
	v_fma_f32 v24, v36, v29, v25
	ds_read_b128 v[40:43], v39 offset:1296
	v_max_f32_e32 v45, 0, v24
	v_fma_f32 v24, v36, v30, v26
	v_fmac_f32_e32 v27, v36, v31
	v_max_f32_e32 v46, 0, v24
	v_max_f32_e32 v47, 0, v27
	ds_read_b128 v[24:27], v39 offset:1088
	ds_read_b128 v[28:31], v39 offset:1344
	s_waitcnt lgkmcnt(2)
	v_fma_f32 v20, v36, v20, v40
	v_fma_f32 v21, v36, v21, v41
	v_max_f32_e32 v20, 0, v20
	v_max_f32_e32 v21, 0, v21
	v_fma_f32 v22, v36, v22, v42
	v_cvt_pk_f16_f32 v42, v20, v21
	s_waitcnt lgkmcnt(0)
	v_fma_f32 v20, v36, v24, v28
	v_fmac_f32_e32 v43, v36, v23
	v_max_f32_e32 v48, 0, v20
	v_fma_f32 v20, v36, v25, v29
	v_max_f32_e32 v22, 0, v22
	v_max_f32_e32 v23, 0, v43
	v_max_f32_e32 v49, 0, v20
	v_fma_f32 v20, v36, v26, v30
	v_cvt_pk_f16_f32 v43, v22, v23
	v_cvt_pk_f16_f32 v41, v46, v47
	v_cvt_pk_f16_f32 v40, v44, v45
	v_max_f32_e32 v50, 0, v20
	ds_read_b128 v[20:23], v39 offset:1104
	ds_read_b128 v[44:47], v39 offset:1360
	v_fmac_f32_e32 v31, v36, v27
	v_max_f32_e32 v51, 0, v31
	ds_read_b128 v[24:27], v39 offset:1152
	ds_read_b128 v[28:31], v39 offset:1408
	v_lshlrev_b32_e32 v94, 4, v92
	s_waitcnt lgkmcnt(2)
	v_fma_f32 v20, v36, v20, v44
	v_fma_f32 v21, v36, v21, v45
	v_max_f32_e32 v20, 0, v20
	v_max_f32_e32 v21, 0, v21
	v_fma_f32 v22, v36, v22, v46
	v_cvt_pk_f16_f32 v46, v20, v21
	s_waitcnt lgkmcnt(0)
	v_fma_f32 v20, v36, v24, v28
	v_fmac_f32_e32 v47, v36, v23
	v_max_f32_e32 v52, 0, v20
	v_fma_f32 v20, v36, v25, v29
	v_max_f32_e32 v22, 0, v22
	v_max_f32_e32 v23, 0, v47
	v_max_f32_e32 v53, 0, v20
	v_fma_f32 v20, v36, v26, v30
	v_cvt_pk_f16_f32 v47, v22, v23
	v_cvt_pk_f16_f32 v45, v50, v51
	v_cvt_pk_f16_f32 v44, v48, v49
	v_max_f32_e32 v54, 0, v20
	ds_read_b128 v[20:23], v39 offset:1168
	ds_read_b128 v[48:51], v39 offset:1424
	v_fmac_f32_e32 v31, v36, v27
	v_max_f32_e32 v55, 0, v31
	ds_read_b128 v[24:27], v39 offset:1216
	ds_read_b128 v[28:31], v39 offset:1472
	v_cvt_pk_f16_f32 v84, v52, v53
	s_waitcnt lgkmcnt(2)
	v_fma_f32 v20, v36, v20, v48
	v_fma_f32 v21, v36, v21, v49
	v_fma_f32 v22, v36, v22, v50
	v_fmac_f32_e32 v51, v36, v23
	v_max_f32_e32 v20, 0, v20
	v_max_f32_e32 v21, 0, v21
	v_max_f32_e32 v22, 0, v22
	v_max_f32_e32 v23, 0, v51
	v_cvt_pk_f16_f32 v87, v22, v23
	v_cvt_pk_f16_f32 v86, v20, v21
	ds_read_b128 v[20:23], v94
	ds_read_b128 v[48:51], v94 offset:1024
	s_waitcnt lgkmcnt(1)
	v_mfma_f32_32x32x16_f16 v[0:15], v[20:23], v[40:43], v[0:15]
	v_fma_f32 v24, v36, v24, v28
	v_max_f32_e32 v52, 0, v24
	v_fma_f32 v24, v36, v25, v29
	v_max_f32_e32 v53, 0, v24
	v_fma_f32 v24, v36, v26, v30
	v_cvt_pk_f16_f32 v85, v54, v55
	v_max_f32_e32 v54, 0, v24
	v_lshlrev_b32_e32 v24, 5, v37
	s_mov_b32 s0, 0x13400
	v_fmac_f32_e32 v31, v36, v27
	v_add3_u32 v28, v24, v38, s0
	ds_read_b128 v[24:27], v94 offset:2048
	s_waitcnt lgkmcnt(1)
	v_mfma_f32_32x32x16_f16 v[0:15], v[48:51], v[44:47], v[0:15]
	v_max_f32_e32 v55, 0, v31
	ds_read_b128 v[20:23], v39 offset:1488
	ds_read_b128 v[88:91], v28
	ds_read_b128 v[28:31], v94 offset:3072
	v_cvt_pk_f16_f32 v37, v54, v55
	v_cmp_gt_u32_e32 vcc, 32, v92
	s_waitcnt lgkmcnt(2)
	v_fma_f32 v20, v36, v32, v20
	v_mfma_f32_32x32x16_f16 v[0:15], v[24:27], v[84:87], v[0:15]
	v_fma_f32 v21, v36, v33, v21
	v_fma_f32 v22, v36, v34, v22
	v_fmac_f32_e32 v23, v36, v35
	v_max_f32_e32 v20, 0, v20
	v_max_f32_e32 v21, 0, v21
	v_max_f32_e32 v22, 0, v22
	v_max_f32_e32 v23, 0, v23
	v_cvt_pk_f16_f32 v39, v22, v23
	v_cvt_pk_f16_f32 v38, v20, v21
	v_cvt_pk_f16_f32 v36, v52, v53
	ds_read_b128 v[20:23], v94 offset:4096
	ds_read_b128 v[32:35], v94 offset:5120
	s_waitcnt lgkmcnt(2)
	v_mfma_f32_32x32x16_f16 v[0:15], v[28:31], v[36:39], v[0:15]
	s_waitcnt lgkmcnt(1)
	v_mfma_f32_32x32x16_f16 v[0:15], v[20:23], v[88:91], v[0:15]
	ds_read_b128 v[20:23], v93 offset:160
	ds_read_b128 v[24:27], v93 offset:192
	ds_read_b128 v[28:31], v93 offset:224
	ds_read_b128 v[64:67], v93 offset:256
	s_waitcnt lgkmcnt(1)
	v_mfma_f32_32x32x16_f16 v[16:31], v[32:35], v[40:43], v[16:31]
	ds_read_b128 v[32:35], v94 offset:6144
	ds_read_b128 v[48:51], v94 offset:7168
	s_nop 3
	v_max_f32_e32 v4, v4, v4
	v_max_f32_e32 v5, v5, v5
	v_max_f32_e32 v6, v6, v6
	v_max_f32_e32 v7, v7, v7
	v_max_f32_e32 v4, 0, v4
	v_max_f32_e32 v5, 0, v5
	s_waitcnt lgkmcnt(1)
	v_mfma_f32_32x32x16_f16 v[16:31], v[32:35], v[44:47], v[16:31]
	v_max_f32_e32 v6, 0, v6
	v_max_f32_e32 v7, 0, v7
	v_max_f32_e32 v2, v2, v2
	v_max_f32_e32 v3, v3, v3
	v_max_f32_e32 v2, 0, v2
	v_max_f32_e32 v3, 0, v3
	v_max_f32_e32 v0, v0, v0
	s_waitcnt lgkmcnt(0)
	v_mfma_f32_32x32x16_f16 v[16:31], v[48:51], v[84:87], v[16:31]
	ds_read_b128 v[32:35], v94 offset:8192
	ds_read_b128 v[48:51], v94 offset:9216
	v_max_f32_e32 v1, v1, v1
	v_max_f32_e32 v0, 0, v0
	v_max_f32_e32 v1, 0, v1
	s_waitcnt lgkmcnt(1)
	v_mfma_f32_32x32x16_f16 v[16:31], v[32:35], v[36:39], v[16:31]
	ds_read_b128 v[32:35], v94 offset:10240
	s_waitcnt lgkmcnt(1)
	v_mfma_f32_32x32x16_f16 v[16:31], v[48:51], v[88:91], v[16:31]
	ds_read_b128 v[68:71], v93 offset:288
	ds_read_b128 v[72:75], v93 offset:320
	ds_read_b128 v[76:79], v93 offset:352
	ds_read_b128 v[48:51], v93 offset:384
	ds_read_b128 v[52:55], v94 offset:11264
	s_waitcnt lgkmcnt(2)
	v_mfma_f32_32x32x16_f16 v[64:79], v[32:35], v[40:43], v[64:79]
	s_waitcnt lgkmcnt(0)
	v_mfma_f32_32x32x16_f16 v[64:79], v[52:55], v[44:47], v[64:79]
	ds_read_b128 v[32:35], v94 offset:12288
	ds_read_b128 v[52:55], v94 offset:13312
	s_waitcnt lgkmcnt(1)
	v_mfma_f32_32x32x16_f16 v[64:79], v[32:35], v[84:87], v[64:79]
	ds_read_b128 v[32:35], v94 offset:14336
	ds_read_b128 v[96:99], v94 offset:15360
	s_waitcnt lgkmcnt(2)
	v_mfma_f32_32x32x16_f16 v[64:79], v[52:55], v[36:39], v[64:79]
	s_waitcnt lgkmcnt(1)
	v_mfma_f32_32x32x16_f16 v[64:79], v[32:35], v[88:91], v[64:79]
	ds_read_b128 v[52:55], v93 offset:416
	ds_read_b128 v[56:59], v93 offset:448
	ds_read_b128 v[60:63], v93 offset:480
	ds_read_b128 v[32:35], v93 offset:512
	s_waitcnt lgkmcnt(1)
	v_mfma_f32_32x32x16_f16 v[48:63], v[96:99], v[40:43], v[48:63]
	ds_read_b128 v[40:43], v94 offset:16384
	ds_read_b128 v[96:99], v94 offset:17408
	s_waitcnt lgkmcnt(1)
	v_mfma_f32_32x32x16_f16 v[48:63], v[40:43], v[44:47], v[48:63]
	ds_read_b128 v[40:43], v94 offset:18432
	ds_read_b128 v[44:47], v94 offset:19456
	s_waitcnt lgkmcnt(2)
	v_mfma_f32_32x32x16_f16 v[48:63], v[96:99], v[84:87], v[48:63]
	v_cvt_pk_f16_f32 v87, v6, v7
	v_cvt_pk_f16_f32 v86, v4, v5
	v_max_f32_e32 v4, v12, v12
	v_max_f32_e32 v5, v13, v13
	v_max_f32_e32 v6, v14, v14
	v_max_f32_e32 v7, v15, v15
	v_max_f32_e32 v4, 0, v4
	s_waitcnt lgkmcnt(1)
	v_mfma_f32_32x32x16_f16 v[48:63], v[40:43], v[36:39], v[48:63]
	v_max_f32_e32 v5, 0, v5
	v_max_f32_e32 v6, 0, v6
	v_max_f32_e32 v7, 0, v7
	v_cvt_pk_f16_f32 v85, v2, v3
	v_max_f32_e32 v2, v10, v10
	v_max_f32_e32 v3, v11, v11
	v_max_f32_e32 v2, 0, v2
	s_waitcnt lgkmcnt(0)
	v_mfma_f32_32x32x16_f16 v[48:63], v[44:47], v[88:91], v[48:63]
	v_cvt_pk_f16_f32 v91, v6, v7
	v_cvt_pk_f16_f32 v90, v4, v5
	v_max_f32_e32 v4, v20, v20
	v_max_f32_e32 v5, v21, v21
	v_max_f32_e32 v6, v22, v22
	v_max_f32_e32 v7, v23, v23
	v_max_f32_e32 v3, 0, v3
	v_max_f32_e32 v4, 0, v4
	v_max_f32_e32 v5, 0, v5
	v_max_f32_e32 v6, 0, v6
	v_max_f32_e32 v7, 0, v7
	v_cvt_pk_f16_f32 v89, v2, v3
	v_max_f32_e32 v2, v18, v18
	v_max_f32_e32 v3, v19, v19
	v_cvt_pk_f16_f32 v19, v6, v7
	v_cvt_pk_f16_f32 v18, v4, v5
	v_max_f32_e32 v4, v28, v28
	v_max_f32_e32 v5, v29, v29
	v_max_f32_e32 v6, v30, v30
	v_max_f32_e32 v7, v31, v31
	v_max_f32_e32 v4, 0, v4
	v_max_f32_e32 v5, 0, v5
	v_max_f32_e32 v6, 0, v6
	v_max_f32_e32 v7, 0, v7
	v_cvt_pk_f16_f32 v84, v0, v1
	v_max_f32_e32 v0, v8, v8
	v_max_f32_e32 v1, v9, v9
	v_cvt_pk_f16_f32 v23, v6, v7
	v_cvt_pk_f16_f32 v22, v4, v5
	v_max_f32_e32 v4, v68, v68
	v_max_f32_e32 v5, v69, v69
	v_max_f32_e32 v6, v70, v70
	v_max_f32_e32 v7, v71, v71
	v_max_f32_e32 v0, 0, v0
	v_max_f32_e32 v1, 0, v1
	v_max_f32_e32 v2, 0, v2
	v_max_f32_e32 v3, 0, v3
	v_max_f32_e32 v4, 0, v4
	v_max_f32_e32 v5, 0, v5
	v_max_f32_e32 v6, 0, v6
	v_max_f32_e32 v7, 0, v7
	v_cvt_pk_f16_f32 v88, v0, v1
	v_max_f32_e32 v0, v16, v16
	v_max_f32_e32 v1, v17, v17
	v_cvt_pk_f16_f32 v17, v2, v3
	v_max_f32_e32 v2, v26, v26
	v_max_f32_e32 v3, v27, v27
	v_cvt_pk_f16_f32 v27, v6, v7
	v_cvt_pk_f16_f32 v26, v4, v5
	ds_read_b128 v[4:7], v94 offset:20480
	v_max_f32_e32 v0, 0, v0
	v_max_f32_e32 v1, 0, v1
	v_cvt_pk_f16_f32 v16, v0, v1
	v_max_f32_e32 v0, v24, v24
	v_max_f32_e32 v1, v25, v25
	v_max_f32_e32 v0, 0, v0
	v_max_f32_e32 v1, 0, v1
	v_cvt_pk_f16_f32 v20, v0, v1
	v_max_f32_e32 v0, v64, v64
	v_max_f32_e32 v1, v65, v65
	ds_read_b128 v[36:39], v93 offset:544
	ds_read_b128 v[40:43], v93 offset:576
	ds_read_b128 v[44:47], v93 offset:608
	v_max_f32_e32 v0, 0, v0
	v_max_f32_e32 v1, 0, v1
	v_cvt_pk_f16_f32 v24, v0, v1
	v_max_f32_e32 v0, v72, v72
	v_max_f32_e32 v2, 0, v2
	v_max_f32_e32 v3, 0, v3
	v_max_f32_e32 v12, 0, v0
	v_max_f32_e32 v0, v73, v73
	v_cvt_pk_f16_f32 v21, v2, v3
	v_max_f32_e32 v2, v66, v66
	v_max_f32_e32 v3, v67, v67
	v_max_f32_e32 v13, 0, v0
	v_max_f32_e32 v0, v74, v74
	v_max_f32_e32 v2, 0, v2
	v_max_f32_e32 v3, 0, v3
	v_max_f32_e32 v14, 0, v0
	v_max_f32_e32 v0, v75, v75
	s_waitcnt lgkmcnt(0)
	v_mfma_f32_32x32x16_f16 v[32:47], v[4:7], v[84:87], v[32:47]
	v_cvt_pk_f16_f32 v25, v2, v3
	v_max_f32_e32 v15, 0, v0
	v_max_f32_e32 v0, v76, v76
	v_max_f32_e32 v1, v77, v77
	v_max_f32_e32 v2, v78, v78
	v_max_f32_e32 v3, v79, v79
	v_max_f32_e32 v0, 0, v0
	v_max_f32_e32 v1, 0, v1
	v_max_f32_e32 v2, 0, v2
	v_max_f32_e32 v3, 0, v3
	v_cvt_pk_f16_f32 v31, v2, v3
	v_cvt_pk_f16_f32 v30, v0, v1
	ds_read_b128 v[0:3], v93 offset:640
	ds_read_b128 v[8:11], v94 offset:21504
	v_max_f32_e32 v4, v48, v48
	v_cvt_pk_f16_f32 v28, v12, v13
	v_max_f32_e32 v12, 0, v4
	v_max_f32_e32 v4, v49, v49
	v_max_f32_e32 v13, 0, v4
	ds_read_b128 v[4:7], v94 offset:22528
	s_waitcnt lgkmcnt(1)
	v_mfma_f32_32x32x16_f16 v[32:47], v[8:11], v[88:91], v[32:47]
	v_max_f32_e32 v8, v50, v50
	v_cvt_pk_f16_f32 v29, v14, v15
	v_max_f32_e32 v14, 0, v8
	v_max_f32_e32 v8, v51, v51
	v_max_f32_e32 v15, 0, v8
	v_max_f32_e32 v8, v52, v52
	v_max_f32_e32 v48, 0, v8
	ds_read_b128 v[8:11], v94 offset:23552
	s_waitcnt lgkmcnt(1)
	v_mfma_f32_32x32x16_f16 v[32:47], v[4:7], v[16:19], v[32:47]
	v_max_f32_e32 v4, v53, v53
	v_max_f32_e32 v49, 0, v4
	v_max_f32_e32 v4, v54, v54
	v_max_f32_e32 v50, 0, v4
	v_max_f32_e32 v4, v55, v55
	v_max_f32_e32 v51, 0, v4
	ds_read_b128 v[4:7], v94 offset:24576
	s_waitcnt lgkmcnt(1)
	v_mfma_f32_32x32x16_f16 v[32:47], v[8:11], v[20:23], v[32:47]
	v_max_f32_e32 v8, v56, v56
	v_cvt_pk_f16_f32 v51, v50, v51
	v_cvt_pk_f16_f32 v50, v48, v49
	v_cvt_pk_f16_f32 v48, v12, v13
	v_max_f32_e32 v12, 0, v8
	ds_read_b128 v[8:11], v94 offset:25600
	v_cvt_pk_f16_f32 v49, v14, v15
	s_waitcnt lgkmcnt(1)
	v_mfma_f32_32x32x16_f16 v[32:47], v[4:7], v[24:27], v[32:47]
	v_max_f32_e32 v4, v57, v57
	v_max_f32_e32 v13, 0, v4
	v_max_f32_e32 v4, v58, v58
	v_max_f32_e32 v14, 0, v4
	v_max_f32_e32 v4, v59, v59
	v_max_f32_e32 v15, 0, v4
	ds_read_b128 v[4:7], v94 offset:26624
	s_waitcnt lgkmcnt(1)
	v_mfma_f32_32x32x16_f16 v[32:47], v[8:11], v[28:31], v[32:47]
	v_max_f32_e32 v8, v60, v60
	v_max_f32_e32 v52, 0, v8
	v_max_f32_e32 v8, v61, v61
	v_max_f32_e32 v53, 0, v8
	v_max_f32_e32 v8, v62, v62
	v_max_f32_e32 v54, 0, v8
	ds_read_b128 v[8:11], v94 offset:27648
	s_waitcnt lgkmcnt(1)
	v_mfma_f32_32x32x16_f16 v[32:47], v[4:7], v[48:51], v[32:47]
	ds_read_b128 v[56:59], v94 offset:28672
	v_max_f32_e32 v4, v63, v63
	v_max_f32_e32 v4, 0, v4
	v_cvt_pk_f16_f32 v55, v54, v4
	v_cvt_pk_f16_f32 v54, v52, v53
	v_cvt_pk_f16_f32 v53, v14, v15
	v_cvt_pk_f16_f32 v52, v12, v13
	s_waitcnt lgkmcnt(1)
	s_nop 0
	v_mfma_f32_32x32x16_f16 v[32:47], v[8:11], v[52:55], v[32:47]
	ds_read_b128 v[4:7], v93 offset:672
	ds_read_b128 v[8:11], v93 offset:704
	ds_read_b128 v[12:15], v93 offset:736
	ds_read_b128 v[60:63], v94 offset:29696
	ds_read_b128 v[64:67], v93 offset:768
	s_waitcnt lgkmcnt(2)
	v_mfma_f32_32x32x16_f16 v[0:15], v[56:59], v[84:87], v[0:15]
	s_waitcnt lgkmcnt(1)
	v_mfma_f32_32x32x16_f16 v[0:15], v[60:63], v[88:91], v[0:15]
	ds_read_b128 v[56:59], v94 offset:30720
	ds_read_b128 v[60:63], v94 offset:31744
	s_waitcnt lgkmcnt(1)
	v_mfma_f32_32x32x16_f16 v[0:15], v[56:59], v[16:19], v[0:15]
	s_waitcnt lgkmcnt(0)
	v_mfma_f32_32x32x16_f16 v[0:15], v[60:63], v[20:23], v[0:15]
	ds_read_b128 v[16:19], v94 offset:32768
	ds_read_b128 v[20:23], v94 offset:33792
	s_waitcnt lgkmcnt(1)
	v_mfma_f32_32x32x16_f16 v[0:15], v[16:19], v[24:27], v[0:15]
	s_waitcnt lgkmcnt(0)
	v_mfma_f32_32x32x16_f16 v[0:15], v[20:23], v[28:31], v[0:15]
	ds_read_b128 v[16:19], v94 offset:34816
	ds_read_b128 v[20:23], v94 offset:35840
	s_waitcnt lgkmcnt(1)
	v_mfma_f32_32x32x16_f16 v[0:15], v[16:19], v[48:51], v[0:15]
	v_max_f32_e32 v16, v32, v32
	v_max_f32_e32 v16, 0, v16
	v_max_f32_e32 v17, v33, v33
	v_fma_f32 v16, v64, v16, 0
	v_max_f32_e32 v17, 0, v17
	v_fmac_f32_e32 v16, v65, v17
	v_max_f32_e32 v17, v34, v34
	s_waitcnt lgkmcnt(0)
	v_mfma_f32_32x32x16_f16 v[0:15], v[20:23], v[52:55], v[0:15]
	v_max_f32_e32 v17, 0, v17
	ds_read_b128 v[18:21], v93 offset:800
	ds_read_b128 v[22:25], v93 offset:832
	v_fmac_f32_e32 v16, v66, v17
	v_max_f32_e32 v17, v35, v35
	v_max_f32_e32 v17, 0, v17
	v_fmac_f32_e32 v16, v67, v17
	v_max_f32_e32 v17, v36, v36
	v_max_f32_e32 v17, 0, v17
	s_waitcnt lgkmcnt(1)
	v_fmac_f32_e32 v16, v18, v17
	v_max_f32_e32 v17, v37, v37
	v_max_f32_e32 v17, 0, v17
	v_fmac_f32_e32 v16, v19, v17
	v_max_f32_e32 v17, v38, v38
	v_max_f32_e32 v17, 0, v17
	v_fmac_f32_e32 v16, v20, v17
	v_max_f32_e32 v17, v39, v39
	v_max_f32_e32 v17, 0, v17
	v_fmac_f32_e32 v16, v21, v17
	v_max_f32_e32 v17, v40, v40
	v_max_f32_e32 v17, 0, v17
	s_waitcnt lgkmcnt(0)
	v_fmac_f32_e32 v16, v22, v17
	v_max_f32_e32 v17, v41, v41
	v_max_f32_e32 v17, 0, v17
	v_fmac_f32_e32 v16, v23, v17
	v_max_f32_e32 v17, v42, v42
	v_max_f32_e32 v17, 0, v17
	ds_read_b128 v[18:21], v93 offset:864
	v_fmac_f32_e32 v16, v24, v17
	v_max_f32_e32 v17, v43, v43
	v_max_f32_e32 v17, 0, v17
	v_fmac_f32_e32 v16, v25, v17
	v_max_f32_e32 v17, v44, v44
	v_max_f32_e32 v17, 0, v17
	ds_read_b128 v[22:25], v93 offset:896
	s_waitcnt lgkmcnt(1)
	v_fmac_f32_e32 v16, v18, v17
	v_max_f32_e32 v17, v45, v45
	v_max_f32_e32 v17, 0, v17
	v_fmac_f32_e32 v16, v19, v17
	v_max_f32_e32 v17, v46, v46
	v_max_f32_e32 v17, 0, v17
	v_fmac_f32_e32 v16, v20, v17
	v_max_f32_e32 v17, v47, v47
	v_max_f32_e32 v17, 0, v17
	v_max_f32_e32 v0, v0, v0
	v_fmac_f32_e32 v16, v21, v17
	v_max_f32_e32 v0, 0, v0
	s_waitcnt lgkmcnt(0)
	v_fmac_f32_e32 v16, v22, v0
	v_max_f32_e32 v0, v1, v1
	v_max_f32_e32 v0, 0, v0
	v_fmac_f32_e32 v16, v23, v0
	v_max_f32_e32 v0, v2, v2
	v_max_f32_e32 v0, 0, v0
	v_fmac_f32_e32 v16, v24, v0
	v_max_f32_e32 v0, v3, v3
	v_max_f32_e32 v17, 0, v0
	ds_read_b128 v[0:3], v93 offset:928
	ds_read_b128 v[18:21], v93 offset:960
	v_max_f32_e32 v4, v4, v4
	v_fmac_f32_e32 v16, v25, v17
	v_max_f32_e32 v4, 0, v4
	s_waitcnt lgkmcnt(1)
	v_fmac_f32_e32 v16, v0, v4
	v_max_f32_e32 v0, v5, v5
	v_max_f32_e32 v0, 0, v0
	v_fmac_f32_e32 v16, v1, v0
	v_max_f32_e32 v0, v6, v6
	v_max_f32_e32 v0, 0, v0
	v_fmac_f32_e32 v16, v2, v0
	v_max_f32_e32 v0, v7, v7
	v_max_f32_e32 v0, 0, v0
	v_fmac_f32_e32 v16, v3, v0
	v_max_f32_e32 v0, v8, v8
	v_max_f32_e32 v0, 0, v0
	s_waitcnt lgkmcnt(0)
	v_fmac_f32_e32 v16, v18, v0
	v_max_f32_e32 v0, v9, v9
	v_max_f32_e32 v0, 0, v0
	v_fmac_f32_e32 v16, v19, v0
	v_max_f32_e32 v0, v10, v10
	v_max_f32_e32 v0, 0, v0
	v_fmac_f32_e32 v16, v20, v0
	v_max_f32_e32 v0, v11, v11
	v_max_f32_e32 v0, 0, v0
	v_fmac_f32_e32 v16, v21, v0
	v_max_f32_e32 v0, v12, v12
	v_max_f32_e32 v0, 0, v0
	v_fmac_f32_e32 v16, v80, v0
	v_max_f32_e32 v0, v13, v13
	v_max_f32_e32 v0, 0, v0
	v_fmac_f32_e32 v16, v81, v0
	v_max_f32_e32 v0, v14, v14
	v_max_f32_e32 v0, 0, v0
	v_fmac_f32_e32 v16, v82, v0
	v_max_f32_e32 v0, v15, v15
	v_max_f32_e32 v0, 0, v0
	v_fmac_f32_e32 v16, v83, v0
	v_mov_b32_e32 v0, v16
	s_nop 1
	v_permlane32_swap_b32_e32 v16, v0
	s_and_saveexec_b64 s[0:1], vcc
	s_cbranch_execz .LBB0_123
	s_mov_b32 s0, s88
	v_add_f32_e32 v0, v16, v0
	s_waitcnt lgkmcnt(0)
	v_add_f32_e32 v0, s0, v0
	v_mul_f32_e32 v0, 0xbfb8aa3b, v0
	v_exp_f32_e32 v1, v0
	s_or_b32 s0, s31, s30
	v_or_b32_e32 v0, s0, v92
	v_add_f32_e32 v2, 1.0, v1
	v_div_scale_f32 v3, s[0:1], v2, v2, 1.0
	v_rcp_f32_e32 v4, v3
	v_div_scale_f32 v5, vcc, 1.0, v2, 1.0
	v_ashrrev_i32_e32 v1, 31, v0
	v_fma_f32 v6, -v3, v4, 1.0
	v_fmac_f32_e32 v4, v6, v4
	v_mul_f32_e32 v6, v5, v4
	v_fma_f32 v7, -v3, v6, v5
	v_fmac_f32_e32 v6, v7, v4
	v_fma_f32 v3, -v3, v6, v5
	v_div_fmas_f32 v3, v3, v4, v6
	v_div_fixup_f32 v2, v3, v2, 1.0
	v_lshl_add_u64 v[0:1], v[0:1], 2, s[22:23]
	global_store_dword v[0:1], v2, off
.LBB0_123:
	s_endpgm
	.section	.rodata,"a",@progbits
	.p2align	6, 0x0
